# P11: final-norm gain vector loaded once before the row loop instead of before every store pair (each reload waited behind the previous nt store's ack)
# baseline (speedup 1.0000x reference)
; DI int opaque_tid() { int t = threadIdx.x; asm volatile("" : "+v"(t)); return t; }
; DI void p11_store(float* out, const float* gf, int row, int lane, const float (&v)[32]) {
;     float ss = 0.f;
; #pragma unroll
;     for (int e = 0; e < 32; ++e) ss += v[e] * v[e];
;     const float r = rsqrtf(wave_sum(ss) * (1.0f / D) + EPS);
; #pragma unroll
;     for (int j = 0; j < 4; ++j) {
;         const int c0 = 512 * j + 8 * lane;
;         const f32x4 g0 = *(const f32x4*)(gf + c0), g1 = *(const f32x4*)(gf + c0 + 4);
;         __builtin_nontemporal_store((f32x4){v[8 * j] * r * g0[0], v[8 * j + 1] * r * g0[1], v[8 * j + 2] * r * g0[2], v[8 * j + 3] * r * g0[3]}, (f32x4*)(out + (size_t)row * D + c0));
;         __builtin_nontemporal_store((f32x4){v[8 * j + 4] * r * g1[0], v[8 * j + 5] * r * g1[1], v[8 * j + 6] * r * g1[2], v[8 * j + 7] * r * g1[3]}, (f32x4*)(out + (size_t)row * D + c0 + 4));
;     }
; }
; DI void p11_final(Frame& F, ArgsP A) {
;     const int ftid = opaque_tid(), flane = ftid & 63;
;     const bf16_t* X1 = (const bf16_t*)(A->ws + WS_X1B); const bf16_t* YK = (const bf16_t*)(A->ws + WS_YK); const float* gf = A->in[17];
;     const int gw = F.vcu * NWAVES + F.wave, NGW = F.G * NWAVES, lane = flane;
;     for (int row = gw; row < T; row += 2 * NGW) {
;         float va[32], vb[32];
;         const int row2 = row + NGW; const bool has2 = row2 < T;
;         p11_load(X1, YK, row, lane, va);
;         if (has2) p11_load(X1, YK, row2, lane, vb);
;         p11_store(A->out, gf, row, lane, va);
;         if (has2) p11_store(A->out, gf, row2, lane, vb);
;     }
; }
.LBB0_1064:
	s_cmp_lt_i32 s60, 12
	s_cselect_b64 s[2:3], -1, 0
	s_cmp_gt_i32 s61, 11
	s_cselect_b64 s[4:5], -1, 0
	s_and_b64 s[2:3], s[2:3], s[4:5]
	s_andn2_b64 vcc, exec, s[2:3]
	s_cbranch_vccnz .LBB0_1072
	s_lshl_b32 s2, s58, 3
	s_add_i32 s2, s2, s59
	s_cmpk_gt_i32 s2, 0x3fff
	s_cbranch_scc1 .LBB0_1072
	v_lshlrev_b32_e32 v1, 3, v0
	s_waitcnt vmcnt(0)
	v_and_b32_e32 v2, 0x1f8, v1
	v_mbcnt_lo_u32_b32 v1, -1, 0
	v_mbcnt_hi_u32_b32 v1, -1, v1
	v_and_b32_e32 v3, 64, v1
	v_add_u32_e32 v3, 64, v3
	v_xor_b32_e32 v4, 1, v1
	v_cmp_lt_i32_e32 vcc, v4, v3
	s_load_dwordx4 s[4:7], s[0:1], 0x88
	s_load_dwordx2 s[10:11], s[0:1], 0x98
	v_cndmask_b32_e32 v4, v1, v4, vcc
	v_lshlrev_b32_e32 v96, 2, v4
	v_xor_b32_e32 v4, 2, v1
	v_cmp_lt_i32_e32 vcc, v4, v3
	v_mov_b32_e32 v5, 0
	v_or_b32_e32 v6, 0x400, v2
	v_cndmask_b32_e32 v4, v1, v4, vcc
	v_lshlrev_b32_e32 v97, 2, v4
	v_xor_b32_e32 v4, 4, v1
	v_cmp_lt_i32_e32 vcc, v4, v3
	v_or_b32_e32 v8, 0x600, v2
	s_lshl_b32 s1, s58, 4
	v_cndmask_b32_e32 v4, v1, v4, vcc
	v_lshlrev_b32_e32 v98, 2, v4
	v_xor_b32_e32 v4, 8, v1
	v_cmp_lt_i32_e32 vcc, v4, v3
	s_lshl_b32 s3, s59, 1
	s_add_i32 s1, s1, s3
	v_cndmask_b32_e32 v4, v1, v4, vcc
	v_lshlrev_b32_e32 v99, 2, v4
	v_xor_b32_e32 v4, 16, v1
	v_cmp_lt_i32_e32 vcc, v4, v3
	s_ashr_i32 s3, s2, 31
	s_lshl_b32 s16, s33, 3
	v_cndmask_b32_e32 v4, v1, v4, vcc
	v_lshlrev_b32_e32 v100, 2, v4
	v_xor_b32_e32 v4, 32, v1
	v_cmp_lt_i32_e32 vcc, v4, v3
	s_lshl_b32 s0, s33, 4
	s_lshl_b32 s17, s33, 5
	v_cndmask_b32_e32 v1, v1, v4, vcc
	v_lshlrev_b32_e32 v4, 2, v2
	s_waitcnt lgkmcnt(0)
	v_lshl_add_u64 v[48:49], s[4:5], 0, v[4:5]
	v_lshlrev_b32_e32 v4, 2, v6
	v_lshl_add_u64 v[50:51], s[4:5], 0, v[4:5]
	v_lshlrev_b32_e32 v4, 2, v8
	v_lshl_add_u64 v[52:53], s[4:5], 0, v[4:5]
	v_lshlrev_b32_e32 v4, 1, v2
	v_lshl_add_u64 v[10:11], s[10:11], 0, v[4:5]
	s_mov_b64 s[4:5], 0x2000000
	v_lshl_add_u64 v[54:55], v[10:11], 0, s[4:5]
	s_or_b32 s4, s1, 1
	s_lshl_b64 s[8:9], s[2:3], 13
	v_and_b32_e32 v3, 63, v0
	s_add_u32 s8, s6, s8
	v_lshlrev_b32_e32 v4, 5, v3
	s_addc_u32 s9, s7, s9
	v_lshlrev_b32_e32 v101, 2, v1
	v_lshl_add_u64 v[0:1], s[8:9], 0, v[4:5]
	s_mov_b64 s[8:9], 0x1810
	s_ashr_i32 s1, s0, 31
	v_lshl_add_u64 v[58:59], v[0:1], 0, s[8:9]
	s_lshl_b64 s[8:9], s[0:1], 13
	s_lshl_b64 s[14:15], s[2:3], 12
	s_add_u32 s10, s10, s14
	v_lshlrev_b32_e32 v4, 4, v3
	s_addc_u32 s11, s11, s15
	s_mov_b64 s[12:13], 0x12200000
	v_lshl_add_u64 v[0:1], s[10:11], 0, v[4:5]
	v_lshl_add_u64 v[56:57], v[10:11], 0, s[12:13]
	v_lshl_add_u64 v[60:61], v[0:1], 0, s[12:13]
	s_lshl_b64 s[10:11], s[0:1], 12
	v_mov_b32_e32 v102, 0x358637bd
	s_mov_b32 s1, 0x800000
	s_movk_i32 s3, 0xf000
	v_lshlrev_b32_e32 v103, 2, v2
	v_lshlrev_b32_e32 v104, 2, v6
	v_lshlrev_b32_e32 v105, 2, v8
	global_load_dwordx4 v[160:163], v[48:49], off offset:16
	global_load_dwordx4 v[164:167], v[48:49], off
	global_load_dwordx4 v[168:171], v[48:49], off offset:2048
	global_load_dwordx4 v[172:175], v[48:49], off offset:2064
	global_load_dwordx4 v[176:179], v[50:51], off
	global_load_dwordx4 v[180:183], v[50:51], off offset:16
	global_load_dwordx4 v[184:187], v[52:53], off
	global_load_dwordx4 v[188:191], v[52:53], off offset:16
	s_waitcnt vmcnt(0)
	s_branch .LBB0_1068

; DI void p11_load(const bf16_t* X1B, const bf16_t* YK, int row, int lane, float (&v)[32]) {
; #pragma unroll
;     for (int j = 0; j < 4; ++j) {
;         const int c0 = 512 * j + 8 * lane;
;         const u32x4 xw = __builtin_nontemporal_load((const u32x4*)(X1B + (size_t)row * D + c0));
;         const f32x4 a0 = {bflo(xw.x), bfhi(xw.x), bflo(xw.y), bfhi(xw.y)}, a1 = {bflo(xw.z), bfhi(xw.z), bflo(xw.w), bfhi(xw.w)};
;         const u32x4 y0 = __builtin_nontemporal_load((const u32x4*)(YK + (size_t)(2 * row) * D + c0)), y1 = __builtin_nontemporal_load((const u32x4*)(YK + (size_t)(2 * row + 1) * D + c0));
;         v[8 * j + 0] = a0[0] + (bflo(y0.x) + bflo(y1.x)); v[8 * j + 1] = a0[1] + (bfhi(y0.x) + bfhi(y1.x)); v[8 * j + 2] = a0[2] + (bflo(y0.y) + bflo(y1.y)); v[8 * j + 3] = a0[3] + (bfhi(y0.y) + bfhi(y1.y));
;         v[8 * j + 4] = a1[0] + (bflo(y0.z) + bflo(y1.z)); v[8 * j + 5] = a1[1] + (bfhi(y0.z) + bfhi(y1.z)); v[8 * j + 6] = a1[2] + (bflo(y0.w) + bflo(y1.w)); v[8 * j + 7] = a1[3] + (bfhi(y0.w) + bfhi(y1.w));
;     }
; }
; DI void p11_store(float* out, const float* gf, int row, int lane, const float (&v)[32]) {
;     float ss = 0.f;
; #pragma unroll
;     for (int e = 0; e < 32; ++e) ss += v[e] * v[e];
.LBB0_1070:
	s_waitcnt vmcnt(9)
	v_lshlrev_b32_e32 v106, 16, v40
	v_and_b32_e32 v107, 0xffff0000, v40
	s_waitcnt vmcnt(7)
	v_lshlrev_b32_e32 v108, 16, v36
	v_and_b32_e32 v109, 0xffff0000, v36
	v_lshlrev_b32_e32 v40, 16, v41
	v_and_b32_e32 v41, 0xffff0000, v41
	v_lshlrev_b32_e32 v36, 16, v37
	v_and_b32_e32 v37, 0xffff0000, v37
	v_lshlrev_b32_e32 v94, 16, v44
	v_and_b32_e32 v95, 0xffff0000, v44
	v_pk_add_f32 v[106:107], v[106:107], v[108:109]
	v_lshlrev_b32_e32 v44, 16, v45
	v_and_b32_e32 v45, 0xffff0000, v45
	v_pk_add_f32 v[36:37], v[40:41], v[36:37]
	v_pk_add_f32 v[94:95], v[106:107], v[94:95]
	v_pk_add_f32 v[36:37], v[36:37], v[44:45]
	v_lshlrev_b32_e32 v44, 16, v42
	v_and_b32_e32 v45, 0xffff0000, v42
	v_lshlrev_b32_e32 v106, 16, v38
	v_and_b32_e32 v107, 0xffff0000, v38
	v_lshlrev_b32_e32 v40, 16, v46
	v_and_b32_e32 v41, 0xffff0000, v46
	v_pk_add_f32 v[44:45], v[44:45], v[106:107]
	v_lshlrev_b32_e32 v42, 16, v43
	v_and_b32_e32 v43, 0xffff0000, v43
	v_lshlrev_b32_e32 v38, 16, v39
	v_and_b32_e32 v39, 0xffff0000, v39
	v_pk_add_f32 v[40:41], v[44:45], v[40:41]
	v_lshlrev_b32_e32 v44, 16, v47
	v_and_b32_e32 v45, 0xffff0000, v47
	v_pk_add_f32 v[38:39], v[42:43], v[38:39]
	s_waitcnt vmcnt(6)
	v_lshlrev_b32_e32 v46, 16, v24
	v_pk_add_f32 v[38:39], v[38:39], v[44:45]
	v_lshlrev_b32_e32 v44, 16, v28
	v_and_b32_e32 v45, 0xffff0000, v28
	v_and_b32_e32 v47, 0xffff0000, v24
	v_lshlrev_b32_e32 v28, 16, v29
	v_and_b32_e32 v29, 0xffff0000, v29
	v_lshlrev_b32_e32 v24, 16, v25
	v_and_b32_e32 v25, 0xffff0000, v25
	v_lshlrev_b32_e32 v42, 16, v32
	v_and_b32_e32 v43, 0xffff0000, v32
	v_pk_add_f32 v[44:45], v[44:45], v[46:47]
	v_lshlrev_b32_e32 v32, 16, v33
	v_and_b32_e32 v33, 0xffff0000, v33
	v_pk_add_f32 v[24:25], v[28:29], v[24:25]
	v_pk_add_f32 v[42:43], v[44:45], v[42:43]
	v_pk_add_f32 v[24:25], v[24:25], v[32:33]
	v_lshlrev_b32_e32 v32, 16, v30
	v_and_b32_e32 v33, 0xffff0000, v30
	v_lshlrev_b32_e32 v44, 16, v26
	v_and_b32_e32 v45, 0xffff0000, v26
	v_lshlrev_b32_e32 v28, 16, v34
	v_and_b32_e32 v29, 0xffff0000, v34
	v_pk_add_f32 v[32:33], v[32:33], v[44:45]
	v_lshlrev_b32_e32 v30, 16, v31
	v_and_b32_e32 v31, 0xffff0000, v31
	v_lshlrev_b32_e32 v26, 16, v27
	v_and_b32_e32 v27, 0xffff0000, v27
	v_pk_add_f32 v[28:29], v[32:33], v[28:29]
	v_lshlrev_b32_e32 v32, 16, v35
	v_and_b32_e32 v33, 0xffff0000, v35
	v_pk_add_f32 v[26:27], v[30:31], v[26:27]
	s_waitcnt vmcnt(1)
	v_lshlrev_b32_e32 v34, 16, v12
	v_pk_add_f32 v[30:31], v[26:27], v[32:33]
	v_lshlrev_b32_e32 v32, 16, v20
	v_and_b32_e32 v33, 0xffff0000, v20
	v_and_b32_e32 v35, 0xffff0000, v12
	v_lshlrev_b32_e32 v26, 16, v16
	v_and_b32_e32 v27, 0xffff0000, v16
	v_pk_add_f32 v[32:33], v[32:33], v[34:35]
	v_lshlrev_b32_e32 v20, 16, v21
	v_and_b32_e32 v21, 0xffff0000, v21
	v_lshlrev_b32_e32 v12, 16, v13
	v_and_b32_e32 v13, 0xffff0000, v13
	v_pk_add_f32 v[26:27], v[32:33], v[26:27]
	v_lshlrev_b32_e32 v16, 16, v17
	v_and_b32_e32 v17, 0xffff0000, v17
	v_pk_add_f32 v[12:13], v[20:21], v[12:13]
	v_lshlrev_b32_e32 v20, 16, v22
	v_and_b32_e32 v21, 0xffff0000, v22
	v_lshlrev_b32_e32 v32, 16, v14
	v_and_b32_e32 v33, 0xffff0000, v14
	v_pk_add_f32 v[16:17], v[12:13], v[16:17]
	v_lshlrev_b32_e32 v12, 16, v18
	v_and_b32_e32 v13, 0xffff0000, v18
	v_pk_add_f32 v[20:21], v[20:21], v[32:33]
	v_lshlrev_b32_e32 v18, 16, v23
	v_pk_add_f32 v[20:21], v[20:21], v[12:13]
	v_lshlrev_b32_e32 v12, 16, v19
	v_and_b32_e32 v13, 0xffff0000, v19
	v_and_b32_e32 v19, 0xffff0000, v23
	v_lshlrev_b32_e32 v14, 16, v15
	v_and_b32_e32 v15, 0xffff0000, v15
	v_pk_add_f32 v[14:15], v[18:19], v[14:15]
	v_lshlrev_b32_e32 v18, 16, v4
	v_and_b32_e32 v19, 0xffff0000, v4
	s_waitcnt vmcnt(0)
	v_lshlrev_b32_e32 v22, 16, v0
	v_and_b32_e32 v23, 0xffff0000, v0
	v_lshlrev_b32_e32 v4, 16, v5
	v_and_b32_e32 v5, 0xffff0000, v5
	v_lshlrev_b32_e32 v0, 16, v1
	v_and_b32_e32 v1, 0xffff0000, v1
	v_pk_add_f32 v[14:15], v[14:15], v[12:13]
	v_lshlrev_b32_e32 v12, 16, v8
	v_and_b32_e32 v13, 0xffff0000, v8
	v_pk_add_f32 v[18:19], v[18:19], v[22:23]
	v_lshlrev_b32_e32 v8, 16, v9
	v_and_b32_e32 v9, 0xffff0000, v9
	v_pk_add_f32 v[0:1], v[4:5], v[0:1]
	v_pk_add_f32 v[12:13], v[18:19], v[12:13]
	v_pk_add_f32 v[0:1], v[0:1], v[8:9]
	v_lshlrev_b32_e32 v8, 16, v6
	v_and_b32_e32 v9, 0xffff0000, v6
	v_lshlrev_b32_e32 v18, 16, v2
	v_and_b32_e32 v19, 0xffff0000, v2
	v_lshlrev_b32_e32 v4, 16, v10
	v_and_b32_e32 v5, 0xffff0000, v10
	v_pk_add_f32 v[8:9], v[8:9], v[18:19]
	v_lshlrev_b32_e32 v6, 16, v7
	v_and_b32_e32 v7, 0xffff0000, v7
	v_lshlrev_b32_e32 v2, 16, v3
	v_and_b32_e32 v3, 0xffff0000, v3
	v_pk_add_f32 v[18:19], v[8:9], v[4:5]
	v_lshlrev_b32_e32 v4, 16, v11
	v_and_b32_e32 v5, 0xffff0000, v11
	v_pk_add_f32 v[2:3], v[6:7], v[2:3]
	v_pk_mul_f32 v[22:23], v[94:95], v[94:95]
	v_pk_add_f32 v[10:11], v[2:3], v[4:5]
	v_pk_mul_f32 v[32:33], v[36:37], v[36:37]
	v_add_f32_e32 v22, v22, v23
	v_add_f32_e32 v22, v32, v22
	v_pk_mul_f32 v[34:35], v[40:41], v[40:41]
	v_add_f32_e32 v22, v33, v22
	v_add_f32_e32 v22, v34, v22
	v_pk_mul_f32 v[44:45], v[38:39], v[38:39]
	v_add_f32_e32 v22, v35, v22
	v_add_f32_e32 v22, v44, v22
	v_pk_mul_f32 v[46:47], v[42:43], v[42:43]
	v_add_f32_e32 v22, v45, v22
	v_add_f32_e32 v22, v46, v22
	v_pk_mul_f32 v[106:107], v[24:25], v[24:25]
	v_add_f32_e32 v22, v47, v22
	v_add_f32_e32 v22, v106, v22
	v_pk_mul_f32 v[108:109], v[28:29], v[28:29]
	v_add_f32_e32 v22, v107, v22
	v_add_f32_e32 v22, v108, v22
	v_pk_mul_f32 v[110:111], v[30:31], v[30:31]
	v_add_f32_e32 v22, v109, v22
	v_add_f32_e32 v22, v110, v22
	v_pk_mul_f32 v[112:113], v[26:27], v[26:27]
	v_add_f32_e32 v22, v111, v22
	v_add_f32_e32 v22, v112, v22
	v_pk_mul_f32 v[114:115], v[16:17], v[16:17]
	v_add_f32_e32 v22, v113, v22
	v_add_f32_e32 v22, v114, v22
	v_pk_mul_f32 v[116:117], v[20:21], v[20:21]
	v_add_f32_e32 v22, v115, v22
	v_add_f32_e32 v22, v116, v22
	v_pk_mul_f32 v[118:119], v[14:15], v[14:15]
	v_add_f32_e32 v22, v117, v22
	v_add_f32_e32 v22, v118, v22
	v_pk_mul_f32 v[120:121], v[12:13], v[12:13]
	v_add_f32_e32 v22, v119, v22
	v_add_f32_e32 v22, v120, v22
	v_pk_mul_f32 v[122:123], v[0:1], v[0:1]
	v_add_f32_e32 v22, v121, v22
	v_add_f32_e32 v22, v122, v22
	v_pk_mul_f32 v[124:125], v[18:19], v[18:19]
	v_add_f32_e32 v22, v123, v22
	v_add_f32_e32 v22, v124, v22
	v_pk_mul_f32 v[126:127], v[10:11], v[10:11]
	v_add_f32_e32 v22, v125, v22
	v_add_f32_e32 v22, v126, v22
	v_add_f32_e32 v22, v127, v22
	ds_bpermute_b32 v23, v96, v22
	s_waitcnt lgkmcnt(0)
; DI void p11_store(float* out, const float* gf, int row, int lane, const float (&v)[32]) {
;     ...
;     const float r = rsqrtf(wave_sum(ss) * (1.0f / D) + EPS);
; #pragma unroll
;     for (int j = 0; j < 4; ++j) {
;         const int c0 = 512 * j + 8 * lane;
;         const f32x4 g0 = *(const f32x4*)(gf + c0), g1 = *(const f32x4*)(gf + c0 + 4);
;         __builtin_nontemporal_store((f32x4){v[8 * j] * r * g0[0], v[8 * j + 1] * r * g0[1], v[8 * j + 2] * r * g0[2], v[8 * j + 3] * r * g0[3]}, (f32x4*)(out + (size_t)row * D + c0));
;         __builtin_nontemporal_store((f32x4){v[8 * j + 4] * r * g1[0], v[8 * j + 5] * r * g1[1], v[8 * j + 6] * r * g1[2], v[8 * j + 7] * r * g1[3]}, (f32x4*)(out + (size_t)row * D + c0 + 4));
;     }
	v_add_f32_e32 v22, v22, v23
	ds_bpermute_b32 v23, v97, v22
	s_waitcnt lgkmcnt(0)
	v_add_f32_e32 v22, v22, v23
	ds_bpermute_b32 v23, v98, v22
	s_waitcnt lgkmcnt(0)
	v_add_f32_e32 v22, v22, v23
	ds_bpermute_b32 v23, v99, v22
	s_waitcnt lgkmcnt(0)
	v_add_f32_e32 v22, v22, v23
	ds_bpermute_b32 v23, v100, v22
	s_waitcnt lgkmcnt(0)
	v_add_f32_e32 v22, v22, v23
	ds_bpermute_b32 v23, v101, v22
	s_waitcnt lgkmcnt(0)
	v_add_f32_e32 v22, v22, v23
	v_fmamk_f32 v22, v22, 0x3a000000, v102
	v_mul_f32_e32 v23, 0x4b800000, v22
	v_cmp_gt_f32_e32 vcc, s1, v22
	s_nop 1
	v_cndmask_b32_e32 v22, v22, v23, vcc
	v_rsq_f32_e32 v22, v22
	s_nop 0
	v_mul_f32_e32 v23, 0x45800000, v22
	v_cndmask_b32_e32 v22, v22, v23, vcc
	v_pk_mul_f32 v[32:33], v[94:95], v[22:23] op_sel_hi:[1,0]
	v_pk_mul_f32 v[34:35], v[36:37], v[22:23] op_sel_hi:[1,0]
	v_pk_mul_f32 v[6:7], v[164:165], v[32:33]
	v_add_co_u32_e32 v32, vcc, s3, v58
	v_pk_mul_f32 v[8:9], v[166:167], v[34:35]
	s_nop 0
	v_addc_co_u32_e32 v33, vcc, -1, v59, vcc
	global_store_dwordx4 v[32:33], v[6:9], off offset:-2064 nt
	v_pk_mul_f32 v[24:25], v[24:25], v[22:23] op_sel_hi:[1,0]
	v_pk_mul_f32 v[34:35], v[42:43], v[22:23] op_sel_hi:[1,0]
	v_pk_mul_f32 v[6:7], v[40:41], v[22:23] op_sel_hi:[1,0]
	v_pk_mul_f32 v[8:9], v[38:39], v[22:23] op_sel_hi:[1,0]
	v_pk_mul_f32 v[2:3], v[160:161], v[6:7]
	v_pk_mul_f32 v[4:5], v[162:163], v[8:9]
	global_store_dwordx4 v[32:33], v[2:5], off offset:-2048 nt
	s_nop 0
	v_pk_mul_f32 v[16:17], v[16:17], v[22:23] op_sel_hi:[1,0]
	v_pk_mul_f32 v[14:15], v[14:15], v[22:23] op_sel_hi:[1,0]
	v_pk_mul_f32 v[20:21], v[20:21], v[22:23] op_sel_hi:[1,0]
	s_andn2_b64 vcc, exec, s[14:15]
	v_pk_mul_f32 v[10:11], v[10:11], v[22:23] op_sel_hi:[1,0]
	v_pk_mul_f32 v[2:3], v[168:169], v[34:35]
	v_pk_mul_f32 v[4:5], v[170:171], v[24:25]
	global_store_dwordx4 v[32:33], v[2:5], off offset:-16 nt
	v_pk_mul_f32 v[24:25], v[26:27], v[22:23] op_sel_hi:[1,0]
	s_nop 0
	v_pk_mul_f32 v[4:5], v[30:31], v[22:23] op_sel_hi:[1,0]
	v_pk_mul_f32 v[2:3], v[28:29], v[22:23] op_sel_hi:[1,0]
	v_pk_mul_f32 v[4:5], v[174:175], v[4:5]
	v_pk_mul_f32 v[2:3], v[172:173], v[2:3]
	global_store_dwordx4 v[58:59], v[2:5], off offset:-4096 nt
	s_nop 0
	s_nop 0
	v_pk_mul_f32 v[2:3], v[176:177], v[24:25]
	v_pk_mul_f32 v[4:5], v[178:179], v[16:17]
	v_pk_mul_f32 v[6:7], v[20:21], v[180:181]
	v_pk_mul_f32 v[8:9], v[14:15], v[182:183]
	global_store_dwordx4 v[58:59], v[2:5], off offset:-2064 nt
	global_store_dwordx4 v[58:59], v[6:9], off offset:-2048 nt
	s_nop 0
	v_pk_mul_f32 v[14:15], v[0:1], v[22:23] op_sel_hi:[1,0]
	v_pk_mul_f32 v[0:1], v[12:13], v[22:23] op_sel_hi:[1,0]
	v_pk_mul_f32 v[12:13], v[18:19], v[22:23] op_sel_hi:[1,0]
	v_pk_mul_f32 v[0:1], v[0:1], v[184:185]
	v_pk_mul_f32 v[2:3], v[14:15], v[186:187]
	v_pk_mul_f32 v[4:5], v[12:13], v[188:189]
	v_pk_mul_f32 v[6:7], v[10:11], v[190:191]
	global_store_dwordx4 v[58:59], v[0:3], off offset:-16 nt
	global_store_dwordx4 v[58:59], v[4:7], off nt
	s_cbranch_vccnz .LBB0_1067
; DI void p11_store(float* out, const float* gf, int row, int lane, const float (&v)[32]) {
;     float ss = 0.f;
; #pragma unroll
;     for (int e = 0; e < 32; ++e) ss += v[e] * v[e];
;     const float r = rsqrtf(wave_sum(ss) * (1.0f / D) + EPS);
; #pragma unroll
;     for (int j = 0; j < 4; ++j) {
;         const int c0 = 512 * j + 8 * lane;
;         const f32x4 g0 = *(const f32x4*)(gf + c0), g1 = *(const f32x4*)(gf + c0 + 4);
;         __builtin_nontemporal_store((f32x4){v[8 * j] * r * g0[0], v[8 * j + 1] * r * g0[1], v[8 * j + 2] * r * g0[2], v[8 * j + 3] * r * g0[3]}, (f32x4*)(out + (size_t)row * D + c0));
;         __builtin_nontemporal_store((f32x4){v[8 * j + 4] * r * g1[0], v[8 * j + 5] * r * g1[1], v[8 * j + 6] * r * g1[2], v[8 * j + 7] * r * g1[3]}, (f32x4*)(out + (size_t)row * D + c0 + 4));
;     }
	v_pk_mul_f32 v[0:1], v[62:63], v[62:63]
	v_pk_mul_f32 v[8:9], v[64:65], v[64:65]
	v_add_f32_e32 v0, v1, v0
	v_add_f32_e32 v8, v8, v0
	v_pk_mul_f32 v[10:11], v[66:67], v[66:67]
	v_add_f32_e32 v8, v9, v8
	v_add_f32_e32 v8, v10, v8
	v_pk_mul_f32 v[12:13], v[68:69], v[68:69]
	v_add_f32_e32 v8, v11, v8
	v_add_f32_e32 v8, v12, v8
	v_pk_mul_f32 v[14:15], v[70:71], v[70:71]
	v_add_f32_e32 v8, v13, v8
	v_add_f32_e32 v8, v14, v8
	v_pk_mul_f32 v[16:17], v[72:73], v[72:73]
	v_add_f32_e32 v8, v15, v8
	v_add_f32_e32 v8, v16, v8
	v_pk_mul_f32 v[18:19], v[74:75], v[74:75]
	v_add_f32_e32 v8, v17, v8
	v_add_f32_e32 v8, v18, v8
	v_pk_mul_f32 v[20:21], v[76:77], v[76:77]
	v_add_f32_e32 v8, v19, v8
	v_add_f32_e32 v8, v20, v8
	v_pk_mul_f32 v[22:23], v[78:79], v[78:79]
	v_add_f32_e32 v8, v21, v8
	v_add_f32_e32 v8, v22, v8
	v_pk_mul_f32 v[24:25], v[80:81], v[80:81]
	v_add_f32_e32 v8, v23, v8
	v_add_f32_e32 v8, v24, v8
	v_pk_mul_f32 v[26:27], v[82:83], v[82:83]
	v_add_f32_e32 v8, v25, v8
	v_add_f32_e32 v8, v26, v8
	v_pk_mul_f32 v[28:29], v[84:85], v[84:85]
	v_add_f32_e32 v8, v27, v8
	v_add_f32_e32 v8, v28, v8
	v_pk_mul_f32 v[30:31], v[86:87], v[86:87]
	v_add_f32_e32 v8, v29, v8
	v_add_f32_e32 v8, v30, v8
	v_pk_mul_f32 v[32:33], v[88:89], v[88:89]
	v_add_f32_e32 v8, v31, v8
	v_add_f32_e32 v8, v32, v8
	v_pk_mul_f32 v[34:35], v[90:91], v[90:91]
	v_add_f32_e32 v8, v33, v8
	v_add_f32_e32 v8, v34, v8
	v_pk_mul_f32 v[36:37], v[92:93], v[92:93]
	v_add_f32_e32 v8, v35, v8
	v_add_f32_e32 v8, v36, v8
	v_add_f32_e32 v8, v37, v8
	ds_bpermute_b32 v9, v96, v8
	s_ashr_i32 s13, s12, 31
	s_lshl_b64 s[12:13], s[12:13], 13
	s_add_u32 s12, s6, s12
	s_addc_u32 s13, s7, s13
	s_waitcnt lgkmcnt(0)
	v_add_f32_e32 v8, v8, v9
	ds_bpermute_b32 v9, v97, v8
	s_waitcnt lgkmcnt(0)
	v_add_f32_e32 v8, v8, v9
	ds_bpermute_b32 v9, v98, v8
	s_waitcnt lgkmcnt(0)
	v_add_f32_e32 v8, v8, v9
	ds_bpermute_b32 v9, v99, v8
	s_waitcnt lgkmcnt(0)
	v_add_f32_e32 v8, v8, v9
	ds_bpermute_b32 v9, v100, v8
	s_waitcnt lgkmcnt(0)
	v_add_f32_e32 v8, v8, v9
	ds_bpermute_b32 v9, v101, v8
	s_waitcnt lgkmcnt(0)
	v_add_f32_e32 v8, v8, v9
	v_fmamk_f32 v8, v8, 0x3a000000, v102
	v_mul_f32_e32 v9, 0x4b800000, v8
	v_cmp_gt_f32_e32 vcc, s1, v8
	s_nop 1
	v_cndmask_b32_e32 v8, v8, v9, vcc
	v_rsq_f32_e32 v8, v8
	s_nop 0
	v_mul_f32_e32 v9, 0x45800000, v8
	v_cndmask_b32_e32 v8, v8, v9, vcc
	v_pk_mul_f32 v[10:11], v[62:63], v[8:9] op_sel_hi:[1,0]
	v_pk_mul_f32 v[12:13], v[64:65], v[8:9] op_sel_hi:[1,0]
	v_pk_mul_f32 v[14:15], v[66:67], v[8:9] op_sel_hi:[1,0]
	v_pk_mul_f32 v[16:17], v[68:69], v[8:9] op_sel_hi:[1,0]
	v_pk_mul_f32 v[6:7], v[166:167], v[12:13]
	v_pk_mul_f32 v[4:5], v[164:165], v[10:11]
	v_pk_mul_f32 v[2:3], v[162:163], v[16:17]
	v_pk_mul_f32 v[0:1], v[160:161], v[14:15]
	global_store_dwordx4 v103, v[4:7], s[12:13] nt
	global_store_dwordx4 v103, v[0:3], s[12:13] offset:16 nt
	s_nop 0
	v_pk_mul_f32 v[10:11], v[72:73], v[8:9] op_sel_hi:[1,0]
	v_pk_mul_f32 v[12:13], v[70:71], v[8:9] op_sel_hi:[1,0]
	v_pk_mul_f32 v[14:15], v[76:77], v[8:9] op_sel_hi:[1,0]
	v_pk_mul_f32 v[16:17], v[74:75], v[8:9] op_sel_hi:[1,0]
	v_pk_mul_f32 v[0:1], v[168:169], v[12:13]
	v_pk_mul_f32 v[2:3], v[170:171], v[10:11]
	v_pk_mul_f32 v[4:5], v[172:173], v[16:17]
	v_pk_mul_f32 v[6:7], v[174:175], v[14:15]
	global_store_dwordx4 v103, v[0:3], s[12:13] offset:2048 nt
	global_store_dwordx4 v103, v[4:7], s[12:13] offset:2064 nt
	s_nop 0
	v_pk_mul_f32 v[10:11], v[80:81], v[8:9] op_sel_hi:[1,0]
	v_pk_mul_f32 v[12:13], v[78:79], v[8:9] op_sel_hi:[1,0]
	v_pk_mul_f32 v[14:15], v[84:85], v[8:9] op_sel_hi:[1,0]
	v_pk_mul_f32 v[16:17], v[82:83], v[8:9] op_sel_hi:[1,0]
	v_pk_mul_f32 v[0:1], v[176:177], v[12:13]
	v_pk_mul_f32 v[2:3], v[178:179], v[10:11]
	v_pk_mul_f32 v[4:5], v[16:17], v[180:181]
	v_pk_mul_f32 v[6:7], v[14:15], v[182:183]
	global_store_dwordx4 v104, v[0:3], s[12:13] nt
	global_store_dwordx4 v104, v[4:7], s[12:13] offset:16 nt
	s_nop 0
	v_pk_mul_f32 v[10:11], v[88:89], v[8:9] op_sel_hi:[1,0]
	v_pk_mul_f32 v[12:13], v[86:87], v[8:9] op_sel_hi:[1,0]
	v_pk_mul_f32 v[14:15], v[92:93], v[8:9] op_sel_hi:[1,0]
	v_pk_mul_f32 v[8:9], v[90:91], v[8:9] op_sel_hi:[1,0]
	v_pk_mul_f32 v[0:1], v[12:13], v[184:185]
	v_pk_mul_f32 v[2:3], v[10:11], v[186:187]
	v_pk_mul_f32 v[4:5], v[8:9], v[188:189]
	v_pk_mul_f32 v[6:7], v[14:15], v[190:191]
	global_store_dwordx4 v105, v[0:3], s[12:13] nt
	global_store_dwordx4 v105, v[4:7], s[12:13] offset:16 nt
	s_branch .LBB0_1067
